# C5 + attention K tile register prefetch 2 tiles deep (second staging set v208-219, loop unrolled x2)
# baseline (speedup 1.0000x reference)
; #define TID() (lnd_s(wv_) * 64 + (int)__builtin_amdgcn_mbcnt_hi(~0u, __builtin_amdgcn_mbcnt_lo(~0u, (unsigned)lnd_s(0))))
; __device__ __forceinline__ int v_rd_base(int lane) { const int g = lane >> 4, c = lane & 15; return (8 * (g >> 1) + (c >> 2)) * KPITCH + (16 * (g & 1) + 4 * (c & 3)) * 2; }
; #define SLOAD(k0) do { \
;     ks0 = *(const bf16x8*)(&Kh[(long)(k0) * LDK + kg[0]]); ks1 = *(const bf16x8*)(&Kh[(long)(k0) * LDK + kg[1]]); ks2 = *(const bf16x8*)(&Kh[(long)(k0) * LDK + kg[2]]); } while (0)
; #define SWRITE(b) do { \
;     *(bf16x8*)(K_lds + (b) * SHM_K + kl[0]) = ks0; *(bf16x8*)(K_lds + (b) * SHM_K + kl[1]) = ks1; *(bf16x8*)(K_lds + (b) * SHM_K + kl[2]) = ks2; } while (0)
; #define SWAIT() asm volatile("s_waitcnt vmcnt(0)" ::: "memory")
; template <int VAR> __device__ __forceinline__ void attn_dense_body(const int wv_, const bf16_t* __restrict__ Qb, const bf16_t* __restrict__ Kh, const bf16_t* __restrict__ Vh, bf16_t* __restrict__ Ob, int seq, unsigned char* lds) {
;     const int tid = TID(), wid = tid >> 6, lane = tid & 63, r32 = lane & 31, hi = lane >> 5;
;     unsigned char* K_lds = lds;
;     float* ws = (float*)(lds + 2 * SHM_K) + wid * 64; float* li_l = ws; float* al_l = ws + 32;
;     float m_reg = -1e30f, l_reg = 0; f32x16 o[4] = {}; bf16x8 qr[12];
;     const bf16_t* Qw = Qb + (long)(wid * QBLK + r32) * LDQ + hi * 8;
; #pragma unroll
;     for (int d0 = 0; d0 < 12; ++d0) qr[d0] = *(const bf16x8*)(Qw + d0 * 16);
;     int kg[3], kl[3];
; #pragma unroll
;     for (int i = 0; i < 3; ++i) { const int id = tid + 512 * i, row = id / 24, ch = id % 24; kg[i] = row * LDK + ch * 8; kl[i] = KSWZ(row, ch * 16); }
;     const int vb0 = (int)(uintptr_t)K_lds + v_rd_base(lane);
;     bf16x8 ks0, ks1, ks2;
;     ...
;     f32x16 p0, p1; float mn, al; bf16x8 pa0, pa1, pa2, pa3; const int NT = seq / KVBLK;
;     SLOAD(0); SWAIT(); SWRITE(0); SLOAD(KVBLK);
;     for (int j = 0; j < NT; ++j) {
;         __syncthreads();
;         if (j + 1 < NT) { SWAIT(); SWRITE((j + 1) & 1); if (j + 2 < NT) SLOAD((j + 2) * KVBLK); }
.LBB0_998:
	v_readlane_b32 s36, v254, 5
	s_mov_b32 s37, 0
	s_lshl_b32 s0, s5, 5
	v_mbcnt_lo_u32_b32 v0, -1, s37
	v_mbcnt_hi_u32_b32 v166, -1, v0
	v_lshl_add_u32 v26, s36, 6, v166
	s_mov_b32 s37, 0x2aaaaaab
	v_mul_hi_i32 v0, v26, s37
	v_lshrrev_b32_e32 v1, 31, v0
	v_ashrrev_i32_e32 v0, 2, v0
	s_and_b32 s0, s0, 0xe0
	s_and_b32 s1, s5, 0xffffff00
	v_add_u32_e32 v27, v0, v1
	v_add_u32_e32 v1, 0x200, v26
	s_or_b32 s0, s0, s1
	s_bfe_u32 s1, s5, 0x50003
	v_mul_hi_i32 v2, v1, s37
	s_or_b32 s2, s0, s1
	v_lshrrev_b32_e32 v3, 31, v2
	v_ashrrev_i32_e32 v2, 2, v2
	s_and_b64 s[0:1], s[42:43], exec
	v_add_u32_e32 v29, v2, v3
	s_cselect_b32 s2, s2, s5
	s_movk_i32 s36, 0xc0
	v_mul_lo_u32 v2, v29, 24
	s_ashr_i32 s44, s2, 4
	v_sub_u32_e32 v30, v1, v2
	v_mul_lo_u32 v1, v29, s36
	s_ashr_i32 s46, s2, 6
	s_ashr_i32 s45, s44, 31
	s_lshl_b32 s2, s2, 8
	v_lshl_add_u32 v2, v30, 3, v1
	v_add_u32_e32 v1, 0x400, v26
	s_lshl_b64 s[0:1], s[44:45], 12
	s_and_b32 s45, s2, 0xf00
	v_mul_hi_i32 v3, v1, s37
	s_or_b32 s0, s0, s45
	v_lshrrev_b32_e32 v4, 31, v3
	v_ashrrev_i32_e32 v3, 2, v3
	s_mulk_i32 s1, 0x180
	s_mul_hi_u32 s2, s0, 0x180
	v_add_u32_e32 v31, v3, v4
	s_add_i32 s1, s2, s1
	s_mulk_i32 s0, 0x180
	v_mul_lo_u32 v0, v27, 24
	v_mul_lo_u32 v3, v31, 24
	s_add_u32 s2, s21, s0
	v_sub_u32_e32 v28, v26, v0
	v_mul_lo_u32 v0, v27, s36
	v_sub_u32_e32 v32, v1, v3
	v_mul_lo_u32 v1, v31, s36
	s_addc_u32 s3, s22, s1
	s_ashr_i32 s47, s46, 31
	s_mul_i32 s38, s46, 0x180000
	v_ashrrev_i32_e32 v170, 6, v26
	v_lshl_add_u32 v0, v28, 3, v0
	v_lshl_add_u32 v8, v32, 3, v1
	s_mul_hi_i32 s29, s46, 0x180000
	s_add_u32 s0, s23, s38
	v_and_b32_e32 v168, 31, v166
	v_lshlrev_b32_e32 v158, 5, v170
	v_ashrrev_i32_e32 v1, 31, v0
	v_ashrrev_i32_e32 v3, 31, v2
	v_ashrrev_i32_e32 v9, 31, v8
	s_addc_u32 s1, s24, s29
	v_bfe_u32 v169, v166, 5, 1
	v_lshlrev_b64 v[12:13], 1, v[0:1]
	v_lshlrev_b64 v[16:17], 1, v[2:3]
	v_lshlrev_b64 v[20:21], 1, v[8:9]
	v_or_b32_e32 v33, v158, v168
	v_mov_b64_e32 v[24:25], s[2:3]
	v_lshl_add_u64 v[14:15], s[0:1], 0, v[12:13]
	v_lshl_add_u64 v[18:19], s[0:1], 0, v[16:17]
	v_lshl_add_u64 v[22:23], s[0:1], 0, v[20:21]
	v_mad_i64_i32 v[24:25], s[0:1], v33, s28, v[24:25]
	v_lshlrev_b32_e32 v96, 4, v169
	v_lshl_add_u64 v[24:25], v[24:25], 0, v[96:97]
	global_load_dwordx4 v[0:3], v[14:15], off
	global_load_dwordx4 v[4:7], v[18:19], off
	global_load_dwordx4 v[8:11], v[22:23], off
	global_load_dwordx4 v[142:145], v[24:25], off
	global_load_dwordx4 v[138:141], v[24:25], off offset:32
	global_load_dwordx4 v[134:137], v[24:25], off offset:64
	global_load_dwordx4 v[130:133], v[24:25], off offset:96
	global_load_dwordx4 v[126:129], v[24:25], off offset:128
	global_load_dwordx4 v[122:125], v[24:25], off offset:160
	global_load_dwordx4 v[118:121], v[24:25], off offset:192
	global_load_dwordx4 v[114:117], v[24:25], off offset:224
	global_load_dwordx4 v[110:113], v[24:25], off offset:256
	global_load_dwordx4 v[106:109], v[24:25], off offset:288
	global_load_dwordx4 v[102:105], v[24:25], off offset:320
	global_load_dwordx4 v[98:101], v[24:25], off offset:352
	s_movk_i32 s0, 0x6000
	v_add_co_u32_e32 v14, vcc, s0, v14
	s_waitcnt vmcnt(0)
	s_movk_i32 s1, 0x190
	s_nop 0
	v_addc_co_u32_e32 v15, vcc, 0, v15, vcc
	v_add_co_u32_e32 v18, vcc, s0, v18
	s_cmp_lg_u32 0, -1
	s_nop 0
	v_addc_co_u32_e32 v19, vcc, 0, v19, vcc
	global_load_dwordx4 v[146:149], v[14:15], off
	global_load_dwordx4 v[150:153], v[18:19], off
	v_add_co_u32_e32 v14, vcc, s0, v22
	v_lshlrev_b32_e32 v18, 2, v166
	s_nop 0
	v_addc_co_u32_e32 v15, vcc, 0, v23, vcc
	global_load_dwordx4 v[154:157], v[14:15], off
	v_and_b32_e32 v14, 0x3fffffc0, v26
	v_lshl_add_u32 v159, v14, 2, 0
	v_mul_lo_u32 v14, v27, s1
	v_lshl_add_u32 v175, v28, 4, v14
	v_mul_lo_u32 v14, v29, s1
	v_lshl_add_u32 v176, v30, 4, v14
	v_mul_lo_u32 v14, v31, s1
	v_lshl_add_u32 v177, v32, 4, v14
	v_lshrrev_b32_e32 v14, 2, v166
	v_and_b32_e32 v15, 16, v166
	v_and_b32_e32 v14, 11, v14
	v_and_or_b32 v15, v18, 12, v15
	v_add_u32_e32 v18, 0, v175
	v_mul_u32_u24_e32 v14, 0x190, v14
	v_lshlrev_b32_e32 v15, 1, v15
	v_mad_u32_u24 v178, v168, s1, v96
	s_cselect_b32 s1, 0, 0
	s_add_u32 s2, s25, s38
	v_add3_u32 v172, v14, s1, v15
	s_addc_u32 s3, s48, s29
	v_mov_b32_e32 v14, v97
	v_mov_b32_e32 v15, v97
	v_and_b32_e32 v167, 63, v166
	v_lshl_add_u64 v[160:161], s[2:3], 0, v[20:21]
	v_lshl_add_u64 v[162:163], s[2:3], 0, v[16:17]
	v_lshl_add_u64 v[164:165], s[2:3], 0, v[12:13]
	global_load_dwordx4 v[208:211], v[164:165], off
	global_load_dwordx4 v[212:215], v[162:163], off
	global_load_dwordx4 v[216:219], v[160:161], off
	v_mov_b32_e32 v12, v97
	v_mov_b32_e32 v13, v97
	s_mov_b32 s0, 0
	v_cmp_gt_u32_e64 s[36:37], 32, v167
	v_lshl_add_u32 v171, v168, 2, v159
	v_mov_b32_e32 v179, 0
	v_mov_b32_e32 v173, 0xf149f2ca
	s_mov_b64 s[2:3], 0x6000
	s_waitcnt vmcnt(6)
	ds_write_b128 v18, v[0:3]
	v_add_u32_e32 v0, 0, v176
	ds_write_b128 v0, v[4:7]
	v_add_u32_e32 v0, 0, v177
	ds_write_b128 v0, v[8:11]
	v_mov_b32_e32 v0, v97
	v_mov_b32_e32 v1, v97
	v_mov_b32_e32 v2, v97
	v_mov_b32_e32 v3, v97
	v_mov_b32_e32 v4, v97
	v_mov_b32_e32 v5, v97
	v_mov_b32_e32 v6, v97
	v_mov_b32_e32 v7, v97
	v_mov_b32_e32 v8, v97
	v_mov_b32_e32 v9, v97
	v_mov_b32_e32 v10, v97
	v_mov_b32_e32 v11, v97
	v_mov_b64_e32 v[62:63], v[14:15]
	v_mov_b64_e32 v[46:47], v[14:15]
	v_mov_b64_e32 v[30:31], v[14:15]
	v_mov_b64_e32 v[60:61], v[12:13]
	v_mov_b64_e32 v[58:59], v[10:11]
	v_mov_b64_e32 v[56:57], v[8:9]
	v_mov_b64_e32 v[54:55], v[6:7]
	v_mov_b64_e32 v[52:53], v[4:5]
	v_mov_b64_e32 v[50:51], v[2:3]
	v_mov_b64_e32 v[48:49], v[0:1]
	v_mov_b64_e32 v[44:45], v[12:13]
	v_mov_b64_e32 v[42:43], v[10:11]
	v_mov_b64_e32 v[40:41], v[8:9]
	v_mov_b64_e32 v[38:39], v[6:7]
	v_mov_b64_e32 v[36:37], v[4:5]
	v_mov_b64_e32 v[34:35], v[2:3]
	v_mov_b64_e32 v[32:33], v[0:1]
	v_mov_b64_e32 v[28:29], v[12:13]
	v_mov_b64_e32 v[26:27], v[10:11]
	v_mov_b64_e32 v[24:25], v[8:9]
	v_mov_b64_e32 v[22:23], v[6:7]
	v_mov_b64_e32 v[20:21], v[4:5]
	v_mov_b64_e32 v[18:19], v[2:3]
	v_mov_b64_e32 v[16:17], v[0:1]
.LBB0_999:
	s_add_i32 s29, s0, 1
	s_bitcmp1_b32 s29, 0
	s_cselect_b32 s1, 0x6400, 0
	s_add_i32 s1, s1, 0
	s_waitcnt lgkmcnt(0)
	s_barrier
	s_cmp_gt_u32 s0, 61
	s_cbranch_scc1 .Ldp_tailwait
	s_waitcnt vmcnt(3)
	s_branch .Ldp_waitdone

; #define SLOAD(k0) do { \
;     ks0 = *(const bf16x8*)(&Kh[(long)(k0) * LDK + kg[0]]); ks1 = *(const bf16x8*)(&Kh[(long)(k0) * LDK + kg[1]]); ks2 = *(const bf16x8*)(&Kh[(long)(k0) * LDK + kg[2]]); } while (0)
; #define SWRITE(b) do { \
;     *(bf16x8*)(K_lds + (b) * SHM_K + kl[0]) = ks0; *(bf16x8*)(K_lds + (b) * SHM_K + kl[1]) = ks1; *(bf16x8*)(K_lds + (b) * SHM_K + kl[2]) = ks2; } while (0)
; #define SWAIT() asm volatile("s_waitcnt vmcnt(0)" ::: "memory")
; template <int VAR> __device__ __forceinline__ void attn_dense_body(const int wv_, const bf16_t* __restrict__ Qb, const bf16_t* __restrict__ Kh, const bf16_t* __restrict__ Vh, bf16_t* __restrict__ Ob, int seq, unsigned char* lds) {
;     ...
;     for (int j = 0; j < NT; ++j) {
;         __syncthreads();
;         if (j + 1 < NT) { SWAIT(); SWRITE((j + 1) & 1); if (j + 2 < NT) SLOAD((j + 2) * KVBLK); }
.Ldp_waitdone:
	v_add_u32_e32 v64, s1, v175
	ds_write_b128 v64, v[146:149]
	v_add_u32_e32 v64, s1, v176
	ds_write_b128 v64, v[150:153]
	v_add_u32_e32 v64, s1, v177
	s_cmp_gt_u32 s0, 60
	ds_write_b128 v64, v[154:157]
	s_cbranch_scc1 .LBB0_1001
	v_lshl_add_u64 v[64:65], v[164:165], 0, s[2:3]
	v_lshl_add_u64 v[66:67], v[162:163], 0, s[2:3]
	global_load_dwordx4 v[146:149], v[64:65], off
	global_load_dwordx4 v[150:153], v[66:67], off
	v_lshl_add_u64 v[64:65], v[160:161], 0, s[2:3]
	global_load_dwordx4 v[154:157], v[64:65], off

; __device__ __forceinline__ void finishSM(f32x16& p0, f32x16& p1, float alpha, float& l_reg, bf16x8& pa0, bf16x8& pa1, bf16x8& pa2, bf16x8& pa3) {
; #pragma unroll
;     for (int r = 0; r < 16; ++r) p1[r] = __builtin_amdgcn_exp2f(p1[r]);
;     float ps = 0;
; #pragma unroll
;     for (int r = 0; r < 16; ++r) ps += p0[r];
; #pragma unroll
;     for (int r = 0; r < 16; ++r) ps += p1[r];
;     { auto rr = __builtin_amdgcn_permlane32_swap(__float_as_uint(ps), __float_as_uint(ps), false, false);
;       ps = __uint_as_float(rr[0]) + __uint_as_float(rr[1]); }
;     l_reg = l_reg * alpha + ps;
;     ...
;     PK4(p0, 0, pa0); PK4(p0, 8, pa1); PK4(p1, 0, pa2); PK4(p1, 8, pa3);
;     ...
; }
; template <int OFF> __device__ __forceinline__ bf16x8 k_read(int kb) { bf16x8 r; asm volatile("ds_read_b128 %0, %1 offset:%2" : "=&v"(r) : "v"(kb), "i"(OFF) : "memory"); return r; }
; __device__ __forceinline__ void qkt(f32x16& p0, f32x16& p1, const unsigned char* Ks, const bf16x8* qr, int r32, int hi) {
;     const int kb = (int)(uintptr_t)Ks + r32 * KPITCH + hi * 16;
;     constexpr int R1 = 32 * KPITCH;
;     p0 = f32x16{}; p1 = f32x16{};
;     bf16x8 a0 = k_read<0>(kb), a1 = k_read<R1>(kb), a2 = k_read<32>(kb), a3 = k_read<R1 + 32>(kb), a4 = k_read<64>(kb), a5 = k_read<R1 + 64>(kb);
;     ...
;     QK_STEP(0, a0, a1, 3, 4); QK_STEP(1, a2, a3, 4, 4); QK_STEP(2, a4, a5, 5, 4);
;     QK_STEP(3, a0, a1, 6, 4); QK_STEP(4, a2, a3, 7, 4); QK_STEP(5, a4, a5, 8, 4);
;     QK_STEP(6, a0, a1, 9, 4); QK_STEP(7, a2, a3, 10, 4); QK_STEP(8, a4, a5, 11, 4);
;     QK_STEP(9, a0, a1, 12, 4); QK_STEP(10, a2, a3, 12, 2); QK_STEP(11, a4, a5, 12, 0);
;     ...
; }
; __device__ __forceinline__ int v_st(int k, int c) { const int kk = (k & ~0xC) | ((k & 4) << 1) | ((k & 8) >> 1); return ((kk >> 3) * 4 + (c >> 5)) * 512 + ((kk & 7) * 32 + (c & 31)) * 2; }
; __device__ __forceinline__ int v_rd_base(int lane) { const int g = lane >> 4, c = lane & 15; return (8 * (g >> 1) + (c >> 2)) * KPITCH + (16 * (g & 1) + 4 * (c & 3)) * 2; }
; template <int OFF> __device__ __forceinline__ s16x4 tr_read(int vb) {
;     s16x4 r; asm volatile("ds_read_b64_tr_b16 %0, %1 offset:%2" : "=&v"(r) : "v"(vb), "i"(OFF) : "memory"); return r;
; }
; __device__ __forceinline__ void pv_d0(f32x16* o, int vb, bf16x8 pa0, bf16x8 pa1, bf16x8 pa2, bf16x8 pa3) {
;     s16x4 a0, a1, a2, a3, a4, a5, a6, a7, b0, b1, b2, b3, b4, b5, b6, b7;
.LBB0_1005:
	v_cndmask_b32_e64 v173, v174, v173, s[38:39]
	v_mul_f32_e32 v174, 0xbdd53b94, v173
	v_mov_b32_e32 v206, v180
	v_fmamk_f32 v80, v80, 0x3dd53b94, v174
	v_fmamk_f32 v81, v81, 0x3dd53b94, v174
	v_fmamk_f32 v82, v82, 0x3dd53b94, v174
	v_fmamk_f32 v83, v83, 0x3dd53b94, v174
	v_fmamk_f32 v84, v84, 0x3dd53b94, v174
	v_fmamk_f32 v85, v85, 0x3dd53b94, v174
	v_fmamk_f32 v86, v86, 0x3dd53b94, v174
	v_fmamk_f32 v87, v87, 0x3dd53b94, v174
	v_exp_f32_e32 v80, v80
	v_exp_f32_e32 v81, v81
	v_exp_f32_e32 v82, v82
	v_exp_f32_e32 v83, v83
	v_exp_f32_e32 v84, v84
	v_exp_f32_e32 v85, v85
	v_exp_f32_e32 v86, v86
	v_exp_f32_e32 v87, v87
	v_add_f32_e32 v204, v80, v81
	v_add_f32_e32 v204, v204, v82
	v_add_f32_e32 v204, v204, v83
	v_add_f32_e32 v204, v204, v84
	v_cvt_pk_bf16_f32 v180, v80, v81
	v_cvt_pk_bf16_f32 v181, v82, v83
	v_cvt_pk_bf16_f32 v182, v84, v85
	v_cvt_pk_bf16_f32 v183, v86, v87
	v_add_f32_e32 v204, v204, v85
	v_add_f32_e32 v204, v204, v86
	v_add_f32_e32 v204, v204, v87
	v_permlane32_swap_b32_e32 v180, v182
	v_permlane32_swap_b32_e32 v181, v183
	s_waitcnt lgkmcnt(8)
	s_nop 1
	v_mfma_f32_32x32x16_bf16 v[0:15], v[180:183], v[220:223], v[0:15]
	v_fmamk_f32 v88, v88, 0x3dd53b94, v174
	v_fmamk_f32 v89, v89, 0x3dd53b94, v174
	v_fmamk_f32 v90, v90, 0x3dd53b94, v174
	v_fmamk_f32 v91, v91, 0x3dd53b94, v174
	v_fmamk_f32 v92, v92, 0x3dd53b94, v174
	v_fmamk_f32 v93, v93, 0x3dd53b94, v174
	v_fmamk_f32 v94, v94, 0x3dd53b94, v174
	v_fmamk_f32 v95, v95, 0x3dd53b94, v174
	v_mfma_f32_32x32x16_bf16 v[48:63], v[180:183], v[224:227], v[48:63]
	v_exp_f32_e32 v88, v88
	v_exp_f32_e32 v89, v89
	v_exp_f32_e32 v90, v90
	v_exp_f32_e32 v91, v91
	v_exp_f32_e32 v92, v92
	v_exp_f32_e32 v93, v93
	v_exp_f32_e32 v94, v94
	v_mfma_f32_32x32x16_bf16 v[32:47], v[180:183], v[228:231], v[32:47]
	v_exp_f32_e32 v95, v95
	v_add_f32_e32 v205, v88, v89
	v_add_f32_e32 v205, v205, v90
	v_add_f32_e32 v205, v205, v91
	v_add_f32_e32 v205, v205, v92
	v_cvt_pk_bf16_f32 v184, v88, v89
	v_cvt_pk_bf16_f32 v185, v90, v91
	v_mfma_f32_32x32x16_bf16 v[16:31], v[180:183], v[232:235], v[16:31]
	v_cvt_pk_bf16_f32 v186, v92, v93
	v_cvt_pk_bf16_f32 v187, v94, v95
	v_add_f32_e32 v205, v205, v93
	v_add_f32_e32 v205, v205, v94
	v_add_f32_e32 v205, v205, v95
	v_permlane32_swap_b32_e32 v184, v186
	v_permlane32_swap_b32_e32 v185, v187
	ds_read_b64_tr_b16 v[220:221], v207 offset:12800
	ds_read_b64_tr_b16 v[222:223], v207 offset:14400
	ds_read_b64_tr_b16 v[224:225], v207 offset:12864
	ds_read_b64_tr_b16 v[226:227], v207 offset:14464
	ds_read_b64_tr_b16 v[228:229], v207 offset:12928
	ds_read_b64_tr_b16 v[230:231], v207 offset:14528
	ds_read_b64_tr_b16 v[232:233], v207 offset:12992
	ds_read_b64_tr_b16 v[234:235], v207 offset:14592
	s_waitcnt lgkmcnt(8)
	v_mfma_f32_32x32x16_bf16 v[0:15], v[184:187], v[236:239], v[0:15]
	v_fmamk_f32 v64, v64, 0x3dd53b94, v174
	v_fmamk_f32 v65, v65, 0x3dd53b94, v174
	v_fmamk_f32 v66, v66, 0x3dd53b94, v174
	v_fmamk_f32 v67, v67, 0x3dd53b94, v174
	v_fmamk_f32 v68, v68, 0x3dd53b94, v174
	v_fmamk_f32 v69, v69, 0x3dd53b94, v174
	v_fmamk_f32 v70, v70, 0x3dd53b94, v174
	v_fmamk_f32 v71, v71, 0x3dd53b94, v174
	v_mfma_f32_32x32x16_bf16 v[48:63], v[184:187], v[240:243], v[48:63]
	v_exp_f32_e32 v64, v64
	v_exp_f32_e32 v65, v65
	v_exp_f32_e32 v66, v66
	v_exp_f32_e32 v67, v67
	v_exp_f32_e32 v68, v68
	v_exp_f32_e32 v69, v69
	v_exp_f32_e32 v70, v70
	v_exp_f32_e32 v71, v71
	v_mfma_f32_32x32x16_bf16 v[32:47], v[184:187], v[244:247], v[32:47]
	v_add_f32_e32 v204, v204, v64
	v_add_f32_e32 v204, v204, v65
	v_add_f32_e32 v204, v204, v66
	v_add_f32_e32 v204, v204, v67
	v_cvt_pk_bf16_f32 v188, v64, v65
	v_cvt_pk_bf16_f32 v189, v66, v67
	v_cvt_pk_bf16_f32 v190, v68, v69
	v_mfma_f32_32x32x16_bf16 v[16:31], v[184:187], v[248:251], v[16:31]
	v_cvt_pk_bf16_f32 v191, v70, v71
	v_add_f32_e32 v204, v204, v68
	v_add_f32_e32 v204, v204, v69
	v_add_f32_e32 v204, v204, v70
	v_add_f32_e32 v204, v204, v71
	v_permlane32_swap_b32_e32 v188, v190
	v_permlane32_swap_b32_e32 v189, v191
	ds_read_b64_tr_b16 v[236:237], v207 offset:19200
	ds_read_b64_tr_b16 v[238:239], v207 offset:20800
	ds_read_b64_tr_b16 v[240:241], v207 offset:19264
	ds_read_b64_tr_b16 v[242:243], v207 offset:20864
	ds_read_b64_tr_b16 v[244:245], v207 offset:19328
	ds_read_b64_tr_b16 v[246:247], v207 offset:20928
	ds_read_b64_tr_b16 v[248:249], v207 offset:19392
	ds_read_b64_tr_b16 v[250:251], v207 offset:20992
	s_waitcnt lgkmcnt(8)
	v_mfma_f32_32x32x16_bf16 v[0:15], v[188:191], v[220:223], v[0:15]
	v_fmamk_f32 v72, v72, 0x3dd53b94, v174
	v_fmamk_f32 v73, v73, 0x3dd53b94, v174
	v_fmamk_f32 v74, v74, 0x3dd53b94, v174
	v_fmamk_f32 v75, v75, 0x3dd53b94, v174
	v_fmamk_f32 v76, v76, 0x3dd53b94, v174
	v_fmamk_f32 v77, v77, 0x3dd53b94, v174
	v_fmamk_f32 v78, v78, 0x3dd53b94, v174
	v_fmamk_f32 v79, v79, 0x3dd53b94, v174
	v_mfma_f32_32x32x16_bf16 v[48:63], v[188:191], v[224:227], v[48:63]
	v_exp_f32_e32 v72, v72
	v_exp_f32_e32 v73, v73
	v_exp_f32_e32 v74, v74
	v_exp_f32_e32 v75, v75
	v_exp_f32_e32 v76, v76
	v_exp_f32_e32 v77, v77
	v_exp_f32_e32 v78, v78
	v_exp_f32_e32 v79, v79
	v_mfma_f32_32x32x16_bf16 v[32:47], v[188:191], v[228:231], v[32:47]
	v_add_f32_e32 v205, v205, v72
	v_add_f32_e32 v205, v205, v73
	v_add_f32_e32 v205, v205, v74
	v_add_f32_e32 v205, v205, v75
	v_cvt_pk_bf16_f32 v192, v72, v73
	v_cvt_pk_bf16_f32 v193, v74, v75
	v_cvt_pk_bf16_f32 v194, v76, v77
	v_mfma_f32_32x32x16_bf16 v[16:31], v[188:191], v[232:235], v[16:31]
	v_cvt_pk_bf16_f32 v195, v78, v79
	v_add_f32_e32 v205, v205, v76
	v_add_f32_e32 v205, v205, v77
	v_add_f32_e32 v205, v205, v78
	v_add_f32_e32 v205, v205, v79
	v_permlane32_swap_b32_e32 v192, v194
	v_permlane32_swap_b32_e32 v193, v195
	s_waitcnt lgkmcnt(0)
	s_nop 1
	v_mfma_f32_32x32x16_bf16 v[0:15], v[192:195], v[236:239], v[0:15]
	v_add_f32_e32 v204, v204, v205
	v_mov_b32_e32 v205, v204
	v_mfma_f32_32x32x16_bf16 v[48:63], v[192:195], v[240:243], v[48:63]
	s_nop 1
	v_permlane32_swap_b32_e32 v204, v205
	v_mfma_f32_32x32x16_bf16 v[32:47], v[192:195], v[244:247], v[32:47]
	v_add_f32_e32 v174, v204, v205
	v_mfma_f32_32x32x16_bf16 v[16:31], v[192:195], v[248:251], v[16:31]
	v_fmac_f32_e32 v174, v179, v206
	s_add_u32 s2, s2, 0x6000
	s_addc_u32 s3, s3, 0
	s_cmp_eq_u32 s2, 0x180000
	s_cbranch_scc1 .LBB0_1007
	s_mov_b32 s0, s29
	v_mov_b32_e32 v179, v174
	s_add_i32 s29, s0, 1
	s_bitcmp1_b32 s29, 0
	s_cselect_b32 s1, 0x6400, 0
	s_add_i32 s1, s1, 0
	s_waitcnt lgkmcnt(0)
	s_barrier
	s_waitcnt vmcnt(3)
	v_add_u32_e32 v64, s1, v175
	ds_write_b128 v64, v[208:211]
	v_add_u32_e32 v64, s1, v176
	ds_write_b128 v64, v[212:215]
	v_add_u32_e32 v64, s1, v177
	s_cmp_gt_u32 s0, 60
	ds_write_b128 v64, v[216:219]
	s_cbranch_scc1 .Ldp_o1001
	v_lshl_add_u64 v[64:65], v[164:165], 0, s[2:3]
	v_lshl_add_u64 v[66:67], v[162:163], 0, s[2:3]
	global_load_dwordx4 v[208:211], v[64:65], off
	global_load_dwordx4 v[212:215], v[66:67], off
	v_lshl_add_u64 v[64:65], v[160:161], 0, s[2:3]
	global_load_dwordx4 v[216:219], v[64:65], off

; __device__ __forceinline__ void finishSM(f32x16& p0, f32x16& p1, float alpha, float& l_reg, bf16x8& pa0, bf16x8& pa1, bf16x8& pa2, bf16x8& pa3) {
; #pragma unroll
;     for (int r = 0; r < 16; ++r) p1[r] = __builtin_amdgcn_exp2f(p1[r]);
;     float ps = 0;
; #pragma unroll
;     for (int r = 0; r < 16; ++r) ps += p0[r];
; #pragma unroll
;     for (int r = 0; r < 16; ++r) ps += p1[r];
;     { auto rr = __builtin_amdgcn_permlane32_swap(__float_as_uint(ps), __float_as_uint(ps), false, false);
;       ps = __uint_as_float(rr[0]) + __uint_as_float(rr[1]); }
;     l_reg = l_reg * alpha + ps;
;     ...
;     PK4(p0, 0, pa0); PK4(p0, 8, pa1); PK4(p1, 0, pa2); PK4(p1, 8, pa3);
;     ...
; }
; template <int OFF> __device__ __forceinline__ bf16x8 k_read(int kb) { bf16x8 r; asm volatile("ds_read_b128 %0, %1 offset:%2" : "=&v"(r) : "v"(kb), "i"(OFF) : "memory"); return r; }
; __device__ __forceinline__ void qkt(f32x16& p0, f32x16& p1, const unsigned char* Ks, const bf16x8* qr, int r32, int hi) {
;     const int kb = (int)(uintptr_t)Ks + r32 * KPITCH + hi * 16;
;     constexpr int R1 = 32 * KPITCH;
;     p0 = f32x16{}; p1 = f32x16{};
;     bf16x8 a0 = k_read<0>(kb), a1 = k_read<R1>(kb), a2 = k_read<32>(kb), a3 = k_read<R1 + 32>(kb), a4 = k_read<64>(kb), a5 = k_read<R1 + 64>(kb);
;     ...
;     QK_STEP(0, a0, a1, 3, 4); QK_STEP(1, a2, a3, 4, 4); QK_STEP(2, a4, a5, 5, 4);
;     QK_STEP(3, a0, a1, 6, 4); QK_STEP(4, a2, a3, 7, 4); QK_STEP(5, a4, a5, 8, 4);
;     QK_STEP(6, a0, a1, 9, 4); QK_STEP(7, a2, a3, 10, 4); QK_STEP(8, a4, a5, 11, 4);
;     QK_STEP(9, a0, a1, 12, 4); QK_STEP(10, a2, a3, 12, 2); QK_STEP(11, a4, a5, 12, 0);
;     ...
; }
; __device__ __forceinline__ int v_st(int k, int c) { const int kk = (k & ~0xC) | ((k & 4) << 1) | ((k & 8) >> 1); return ((kk >> 3) * 4 + (c >> 5)) * 512 + ((kk & 7) * 32 + (c & 31)) * 2; }
; __device__ __forceinline__ int v_rd_base(int lane) { const int g = lane >> 4, c = lane & 15; return (8 * (g >> 1) + (c >> 2)) * KPITCH + (16 * (g & 1) + 4 * (c & 3)) * 2; }
; template <int OFF> __device__ __forceinline__ s16x4 tr_read(int vb) {
;     s16x4 r; asm volatile("ds_read_b64_tr_b16 %0, %1 offset:%2" : "=&v"(r) : "v"(vb), "i"(OFF) : "memory"); return r;
; }
; __device__ __forceinline__ void pv_d0(f32x16* o, int vb, bf16x8 pa0, bf16x8 pa1, bf16x8 pa2, bf16x8 pa3) {
;     s16x4 a0, a1, a2, a3, a4, a5, a6, a7, b0, b1, b2, b3, b4, b5, b6, b7;
.Ldp_o1005:
	v_cndmask_b32_e64 v173, v174, v173, s[38:39]
	v_mul_f32_e32 v174, 0xbdd53b94, v173
	v_mov_b32_e32 v206, v180
	v_fmamk_f32 v80, v80, 0x3dd53b94, v174
	v_fmamk_f32 v81, v81, 0x3dd53b94, v174
	v_fmamk_f32 v82, v82, 0x3dd53b94, v174
	v_fmamk_f32 v83, v83, 0x3dd53b94, v174
	v_fmamk_f32 v84, v84, 0x3dd53b94, v174
	v_fmamk_f32 v85, v85, 0x3dd53b94, v174
	v_fmamk_f32 v86, v86, 0x3dd53b94, v174
	v_fmamk_f32 v87, v87, 0x3dd53b94, v174
	v_exp_f32_e32 v80, v80
	v_exp_f32_e32 v81, v81
	v_exp_f32_e32 v82, v82
	v_exp_f32_e32 v83, v83
	v_exp_f32_e32 v84, v84
	v_exp_f32_e32 v85, v85
	v_exp_f32_e32 v86, v86
	v_exp_f32_e32 v87, v87
	v_add_f32_e32 v204, v80, v81
	v_add_f32_e32 v204, v204, v82
	v_add_f32_e32 v204, v204, v83
	v_add_f32_e32 v204, v204, v84
	v_cvt_pk_bf16_f32 v180, v80, v81
	v_cvt_pk_bf16_f32 v181, v82, v83
	v_cvt_pk_bf16_f32 v182, v84, v85
	v_cvt_pk_bf16_f32 v183, v86, v87
	v_add_f32_e32 v204, v204, v85
	v_add_f32_e32 v204, v204, v86
	v_add_f32_e32 v204, v204, v87
	v_permlane32_swap_b32_e32 v180, v182
	v_permlane32_swap_b32_e32 v181, v183
	s_waitcnt lgkmcnt(8)
	s_nop 1
	v_mfma_f32_32x32x16_bf16 v[0:15], v[180:183], v[220:223], v[0:15]
	v_fmamk_f32 v88, v88, 0x3dd53b94, v174
	v_fmamk_f32 v89, v89, 0x3dd53b94, v174
	v_fmamk_f32 v90, v90, 0x3dd53b94, v174
	v_fmamk_f32 v91, v91, 0x3dd53b94, v174
	v_fmamk_f32 v92, v92, 0x3dd53b94, v174
	v_fmamk_f32 v93, v93, 0x3dd53b94, v174
	v_fmamk_f32 v94, v94, 0x3dd53b94, v174
	v_fmamk_f32 v95, v95, 0x3dd53b94, v174
	v_mfma_f32_32x32x16_bf16 v[48:63], v[180:183], v[224:227], v[48:63]
	v_exp_f32_e32 v88, v88
	v_exp_f32_e32 v89, v89
	v_exp_f32_e32 v90, v90
	v_exp_f32_e32 v91, v91
	v_exp_f32_e32 v92, v92
	v_exp_f32_e32 v93, v93
	v_exp_f32_e32 v94, v94
	v_mfma_f32_32x32x16_bf16 v[32:47], v[180:183], v[228:231], v[32:47]
	v_exp_f32_e32 v95, v95
	v_add_f32_e32 v205, v88, v89
	v_add_f32_e32 v205, v205, v90
	v_add_f32_e32 v205, v205, v91
	v_add_f32_e32 v205, v205, v92
	v_cvt_pk_bf16_f32 v184, v88, v89
	v_cvt_pk_bf16_f32 v185, v90, v91
	v_mfma_f32_32x32x16_bf16 v[16:31], v[180:183], v[232:235], v[16:31]
	v_cvt_pk_bf16_f32 v186, v92, v93
	v_cvt_pk_bf16_f32 v187, v94, v95
	v_add_f32_e32 v205, v205, v93
	v_add_f32_e32 v205, v205, v94
	v_add_f32_e32 v205, v205, v95
	v_permlane32_swap_b32_e32 v184, v186
	v_permlane32_swap_b32_e32 v185, v187
	ds_read_b64_tr_b16 v[220:221], v207 offset:12800
	ds_read_b64_tr_b16 v[222:223], v207 offset:14400
	ds_read_b64_tr_b16 v[224:225], v207 offset:12864
	ds_read_b64_tr_b16 v[226:227], v207 offset:14464
	ds_read_b64_tr_b16 v[228:229], v207 offset:12928
	ds_read_b64_tr_b16 v[230:231], v207 offset:14528
	ds_read_b64_tr_b16 v[232:233], v207 offset:12992
	ds_read_b64_tr_b16 v[234:235], v207 offset:14592
	s_waitcnt lgkmcnt(8)
	v_mfma_f32_32x32x16_bf16 v[0:15], v[184:187], v[236:239], v[0:15]
	v_fmamk_f32 v64, v64, 0x3dd53b94, v174
	v_fmamk_f32 v65, v65, 0x3dd53b94, v174
	v_fmamk_f32 v66, v66, 0x3dd53b94, v174
	v_fmamk_f32 v67, v67, 0x3dd53b94, v174
	v_fmamk_f32 v68, v68, 0x3dd53b94, v174
	v_fmamk_f32 v69, v69, 0x3dd53b94, v174
	v_fmamk_f32 v70, v70, 0x3dd53b94, v174
	v_fmamk_f32 v71, v71, 0x3dd53b94, v174
	v_mfma_f32_32x32x16_bf16 v[48:63], v[184:187], v[240:243], v[48:63]
	v_exp_f32_e32 v64, v64
	v_exp_f32_e32 v65, v65
	v_exp_f32_e32 v66, v66
	v_exp_f32_e32 v67, v67
	v_exp_f32_e32 v68, v68
	v_exp_f32_e32 v69, v69
	v_exp_f32_e32 v70, v70
	v_exp_f32_e32 v71, v71
	v_mfma_f32_32x32x16_bf16 v[32:47], v[184:187], v[244:247], v[32:47]
	v_add_f32_e32 v204, v204, v64
	v_add_f32_e32 v204, v204, v65
	v_add_f32_e32 v204, v204, v66
	v_add_f32_e32 v204, v204, v67
	v_cvt_pk_bf16_f32 v188, v64, v65
	v_cvt_pk_bf16_f32 v189, v66, v67
	v_cvt_pk_bf16_f32 v190, v68, v69
	v_mfma_f32_32x32x16_bf16 v[16:31], v[184:187], v[248:251], v[16:31]
	v_cvt_pk_bf16_f32 v191, v70, v71
	v_add_f32_e32 v204, v204, v68
	v_add_f32_e32 v204, v204, v69
	v_add_f32_e32 v204, v204, v70
	v_add_f32_e32 v204, v204, v71
	v_permlane32_swap_b32_e32 v188, v190
	v_permlane32_swap_b32_e32 v189, v191
	ds_read_b64_tr_b16 v[236:237], v207 offset:19200
	ds_read_b64_tr_b16 v[238:239], v207 offset:20800
	ds_read_b64_tr_b16 v[240:241], v207 offset:19264
	ds_read_b64_tr_b16 v[242:243], v207 offset:20864
	ds_read_b64_tr_b16 v[244:245], v207 offset:19328
	ds_read_b64_tr_b16 v[246:247], v207 offset:20928
	ds_read_b64_tr_b16 v[248:249], v207 offset:19392
	ds_read_b64_tr_b16 v[250:251], v207 offset:20992
	s_waitcnt lgkmcnt(8)
	v_mfma_f32_32x32x16_bf16 v[0:15], v[188:191], v[220:223], v[0:15]
	v_fmamk_f32 v72, v72, 0x3dd53b94, v174
	v_fmamk_f32 v73, v73, 0x3dd53b94, v174
	v_fmamk_f32 v74, v74, 0x3dd53b94, v174
	v_fmamk_f32 v75, v75, 0x3dd53b94, v174
	v_fmamk_f32 v76, v76, 0x3dd53b94, v174
	v_fmamk_f32 v77, v77, 0x3dd53b94, v174
	v_fmamk_f32 v78, v78, 0x3dd53b94, v174
	v_fmamk_f32 v79, v79, 0x3dd53b94, v174
	v_mfma_f32_32x32x16_bf16 v[48:63], v[188:191], v[224:227], v[48:63]
	v_exp_f32_e32 v72, v72
	v_exp_f32_e32 v73, v73
	v_exp_f32_e32 v74, v74
	v_exp_f32_e32 v75, v75
	v_exp_f32_e32 v76, v76
	v_exp_f32_e32 v77, v77
	v_exp_f32_e32 v78, v78
	v_exp_f32_e32 v79, v79
	v_mfma_f32_32x32x16_bf16 v[32:47], v[188:191], v[228:231], v[32:47]
	v_add_f32_e32 v205, v205, v72
	v_add_f32_e32 v205, v205, v73
	v_add_f32_e32 v205, v205, v74
	v_add_f32_e32 v205, v205, v75
	v_cvt_pk_bf16_f32 v192, v72, v73
	v_cvt_pk_bf16_f32 v193, v74, v75
	v_cvt_pk_bf16_f32 v194, v76, v77
	v_mfma_f32_32x32x16_bf16 v[16:31], v[188:191], v[232:235], v[16:31]
	v_cvt_pk_bf16_f32 v195, v78, v79
	v_add_f32_e32 v205, v205, v76
	v_add_f32_e32 v205, v205, v77
	v_add_f32_e32 v205, v205, v78
	v_add_f32_e32 v205, v205, v79
	v_permlane32_swap_b32_e32 v192, v194
	v_permlane32_swap_b32_e32 v193, v195
	s_waitcnt lgkmcnt(0)
	s_nop 1
	v_mfma_f32_32x32x16_bf16 v[0:15], v[192:195], v[236:239], v[0:15]
	v_add_f32_e32 v204, v204, v205
	v_mov_b32_e32 v205, v204
	v_mfma_f32_32x32x16_bf16 v[48:63], v[192:195], v[240:243], v[48:63]
	s_nop 1
	v_permlane32_swap_b32_e32 v204, v205
	v_mfma_f32_32x32x16_bf16 v[32:47], v[192:195], v[244:247], v[32:47]
	v_add_f32_e32 v174, v204, v205
	v_mfma_f32_32x32x16_bf16 v[16:31], v[192:195], v[248:251], v[16:31]
	v_fmac_f32_e32 v174, v179, v206
	s_add_u32 s2, s2, 0x6000
	s_addc_u32 s3, s3, 0
	s_cmp_eq_u32 s2, 0x180000
	s_mov_b32 s0, s29
	v_mov_b32_e32 v179, v174
	s_branch .LBB0_999

; __device__ __forceinline__ void xcd_barrier_complete(unsigned* bar, unsigned x, unsigned& nloc, unsigned& nx) {
;     const unsigned G = gridDim.x * gridDim.y * gridDim.z;
;     unsigned sum, cnt, mine, sp = 0u;
; __device__ __forceinline__ void xcd_barrier(const XcdBarrier& b, const bool t0) {
;     asm volatile("s_waitcnt vmcnt(0)" ::: "memory");
;     __syncthreads();
;     if (t0) {
;         unsigned* bar = b.bar;
;         __builtin_amdgcn_s_waitcnt(0);
;         unsigned nloc = b.st[0], nx = b.st[1];
;         if (nloc == 0u) { xcd_barrier_complete(bar, b.x, nloc, nx); b.st[0] = nloc; b.st[1] = nx; }
.LBB0_1013:
	v_mov_b32_e32 v216, 1
	v_mov_b32_e32 v217, 0x358637bd
	v_mov_b32_e32 v218, 1.0
	v_readlane_b32 s20, v254, 3
	v_readlane_b32 s21, v254, 4
	s_cmp_ge_i32 s26, s21
	s_cbranch_scc1 .LBB0_1063
	v_readlane_b32 s0, v254, 5
	s_mov_b32 s1, s27
	s_waitcnt vmcnt(0)
	s_lshl_b32 s0, s0, 6
	v_mbcnt_lo_u32_b32 v0, -1, s1
	v_mbcnt_hi_u32_b32 v0, -1, v0
	v_sub_u32_e32 v0, 0, v0
	v_cmp_eq_u32_e32 vcc, s0, v0
	s_waitcnt vmcnt(0)
	s_barrier
	s_and_saveexec_b64 s[2:3], vcc
	s_cbranch_execz .LBB0_1062
	v_readlane_b32 s0, v254, 52
	s_waitcnt vmcnt(0) expcnt(0) lgkmcnt(0)
	s_nop 0
	v_mov_b32_e32 v0, s0
	ds_read_b32 v2, v0
	v_readlane_b32 s0, v254, 53
	s_waitcnt lgkmcnt(0)
	v_cmp_ne_u32_e32 vcc, 0, v2
	v_mov_b32_e32 v0, s0
	ds_read_b32 v0, v0
	s_cbranch_vccnz .LBB0_1030
	s_load_dwordx2 s[0:1], s[18:19], 0x4
	s_mov_b32 s23, 1
	s_waitcnt lgkmcnt(0)
	s_mul_i32 s22, s0, s4
	s_mul_i32 s22, s22, s1
	s_branch .LBB0_1018
